# FoX forget prefix spread over all 512 half-workgroups (segment totals published with flags at phase start, offsets + cumulative sums at phase end) instead of 32 half-workgroups reading 512 KiB each
# speedup vs baseline: 1.0111x; 1.0038x over previous
; DI int tidx() { int t = threadIdx.x & 255; asm volatile("" : "+v"(t)); return t; }
; DI float bflo(unsigned u) { return __uint_as_float(u << 16); }
; DI float bfhi(unsigned u) { return __uint_as_float(u & 0xffff0000u); }
; DI void phase_foxcum(const Params& p, int bid, int nb, char* lds) {
;     ...
;   for (int bh = bid; bh < 32; bh += nb) {
;     const int b = bh >> 3, h = bh & 7;
;     float v[32]; float run = 0.f;
; #pragma unroll
;     for (int i = 0; i < 32; ++i) { run += small[((size_t)b * S_ + tid * 32 + i) * 16 + h]; v[i] = run; }
;     tot[tid] = run; __syncthreads();
;     float off = 0.f; for (int j = 0; j < tid; ++j) off += tot[j];
; #pragma unroll
;     for (int i = 0; i < 32; ++i) fneg[(size_t)bh * S_ + tid * 32 + i] = -(v[i] + off) * LOG2E;
;     __syncthreads();
;   }
; }
; DI void phase_qknorm(const Params& p, int bid, int nb) {
;   const int lane = tidx() & 63, gw = bid * 4 + (tidx() >> 6), nw = nb * 4;
;   const bf16_t* proj = (const bf16_t*)(p.ws + WS_P);
;   unsigned* qk = (unsigned*)(p.ws + WS_CTL) + 64;
;   for (int it = gw; it < 4096; it += nw) {
;     const int bh = it >> 7, j = it & 127, b = bh >> 3, h = bh & 7;
;     const bf16_t* rp = proj + ((size_t)b * S_ + j * 64 + lane) * PP + h * 64;
;     float sq = 0.f, sk = 0.f;
; #pragma unroll
;     for (int q = 0; q < 8; ++q) { const u32x4 wq = *(const u32x4*)(rp + 8 * q), wk = *(const u32x4*)(rp + 512 + 8 * q);
; #pragma unroll
;       for (int e = 0; e < 4; ++e) { const float a0 = bflo(wq[e]), a1 = bfhi(wq[e]), c0 = bflo(wk[e]), c1 = bfhi(wk[e]); sq += a0 * a0 + a1 * a1; sk += c0 * c0 + c1 * c1; } }
; #pragma unroll
;     for (int d = 32; d >= 1; d >>= 1) { sq = fmaxf(sq, __shfl_xor(sq, d)); sk = fmaxf(sk, __shfl_xor(sk, d)); }
.LBB0_1068:
	s_or_b64 exec, exec, s[0:1]
	v_cmp_gt_i32_e64 s[6:7], 32, v176
	s_waitcnt lgkmcnt(0)
	s_barrier
	v_readfirstlane_b32 s4, v176
	v_readfirstlane_b32 s5, v206
	s_lshr_b32 s5, s5, 6
	v_mbcnt_lo_u32_b32 v0, -1, 0
	v_mbcnt_hi_u32_b32 v0, -1, v0
	v_lshrrev_b32_e32 v1, 5, v0
	v_and_b32_e32 v2, 31, v0
	v_lshl_add_u32 v3, s5, 1, v1
	s_lshl_b32 s6, s4, 6
	v_lshl_add_u32 v4, v2, 1, s6
	v_lshlrev_b32_e32 v4, 6, v4
	v_lshl_add_u32 v4, v3, 2, v4
	s_add_u32 s8, s84, 0x1700000
	s_addc_u32 s9, s85, 0
	global_load_dword v5, v4, s[8:9]
	global_load_dword v6, v4, s[8:9] offset:64
	s_waitcnt vmcnt(0)
	v_add_f32_e32 v8, v5, v6
	s_nop 1
	v_add_f32_dpp v8, v8, v8 row_shr:1 row_mask:0xf bank_mask:0xf bound_ctrl:1
	s_nop 1
	v_add_f32_dpp v8, v8, v8 row_shr:2 row_mask:0xf bank_mask:0xf bound_ctrl:1
	s_nop 1
	v_add_f32_dpp v8, v8, v8 row_shr:4 row_mask:0xf bank_mask:0xf bound_ctrl:1
	s_nop 1
	v_add_f32_dpp v8, v8, v8 row_shr:8 row_mask:0xf bank_mask:0xf bound_ctrl:1
	s_nop 1
	v_add_f32_dpp v8, v8, v8 row_bcast:15 row_mask:0xa bank_mask:0xf
	v_mov_b32_e32 v9, 1
	s_lshl_b32 s6, s4, 6
	v_lshl_add_u32 v7, v3, 3, s6
	s_add_u32 s12, s84, 0x8000
	s_addc_u32 s13, s85, 0
	v_cmp_eq_u32_e32 vcc, 31, v2
	s_and_saveexec_b64 s[14:15], vcc
	global_store_dwordx2 v7, v[8:9], s[12:13] sc0 sc1
	s_or_b64 exec, exec, s[14:15]
.LBB0_1081:
	v_mov_b32_e32 v0, v206
	v_mov_b32_e32 v1, v206
	s_movk_i32 s0, 0x1000
	v_ashrrev_i32_e32 v1, 6, v1
	v_lshl_add_u32 v17, v176, 2, v1
	v_cmp_gt_i32_e32 vcc, s0, v17
	s_and_saveexec_b64 s[4:5], vcc
	s_cbranch_execz .LBB0_1086
	v_and_b32_e32 v16, 63, v0
	v_mbcnt_hi_u32_b32 v0, -1, v177
	v_and_b32_e32 v1, 64, v0
	v_add_u32_e32 v1, 64, v1
	v_xor_b32_e32 v2, 32, v0
	v_cmp_lt_i32_e64 s[0:1], v2, v1
	s_lshl_b32 s2, s86, 3
	v_mov_b32_e32 v19, 0
	v_cndmask_b32_e64 v2, v0, v2, s[0:1]
	v_lshlrev_b32_e32 v24, 2, v2
	v_xor_b32_e32 v2, 16, v0
	v_cmp_lt_i32_e64 s[0:1], v2, v1
	v_cmp_eq_u32_e32 vcc, 0, v16
	v_lshlrev_b32_e32 v30, 6, v17
	v_cndmask_b32_e64 v2, v0, v2, s[0:1]
	v_lshlrev_b32_e32 v25, 2, v2
	v_xor_b32_e32 v2, 8, v0
	v_cmp_lt_i32_e64 s[0:1], v2, v1
	s_lshl_b32 s3, s86, 9
	s_mov_b64 s[8:9], 0
	v_cndmask_b32_e64 v2, v0, v2, s[0:1]
	v_lshlrev_b32_e32 v26, 2, v2
	v_xor_b32_e32 v2, 4, v0
	v_cmp_lt_i32_e64 s[0:1], v2, v1
	s_movk_i32 s10, 0x2c00
	v_mov_b64_e32 v[20:21], s[58:59]
	v_cndmask_b32_e64 v2, v0, v2, s[0:1]
	v_lshlrev_b32_e32 v27, 2, v2
	v_xor_b32_e32 v2, 2, v0
	v_cmp_lt_i32_e64 s[0:1], v2, v1
	s_movk_i32 s11, 0xfff
	s_nop 0
	v_cndmask_b32_e64 v2, v0, v2, s[0:1]
	v_lshlrev_b32_e32 v28, 2, v2
	v_xor_b32_e32 v2, 1, v0
	v_cmp_lt_i32_e64 s[0:1], v2, v1
	s_nop 1
	v_cndmask_b32_e64 v0, v0, v2, s[0:1]
	v_lshlrev_b32_e32 v29, 2, v0
	s_branch .LBB0_1084

; DI void phase_foxcum(const Params& p, int bid, int nb, char* lds) {
;     ...
;     float v[32]; float run = 0.f;
; #pragma unroll
;     for (int i = 0; i < 32; ++i) { run += small[((size_t)b * S_ + tid * 32 + i) * 16 + h]; v[i] = run; }
;     tot[tid] = run; __syncthreads();
;     float off = 0.f; for (int j = 0; j < tid; ++j) off += tot[j];
; #pragma unroll
;     for (int i = 0; i < 32; ++i) fneg[(size_t)bh * S_ + tid * 32 + i] = -(v[i] + off) * LOG2E;
; DI void xcd_barrier(const XcdBarrier& b) {
;   asm volatile("s_waitcnt vmcnt(0)" ::: "memory");
;   __syncthreads();
;   if (threadIdx.x == 0) {
;     unsigned* bar = b.bar;
;     __builtin_amdgcn_s_waitcnt(0);
;     unsigned nloc = b.st[0], nx = b.st[1];
;     if (nloc == 0u) { xcd_barrier_complete(bar, b.x, nloc, nx); b.st[0] = nloc; b.st[1] = nx; }
.LBB0_1155:
	s_or_b64 exec, exec, s[16:17]
	v_readfirstlane_b32 s26, v176
	v_readfirstlane_b32 s27, v206
	s_lshr_b32 s27, s27, 6
	v_mbcnt_lo_u32_b32 v0, -1, 0
	v_mbcnt_hi_u32_b32 v0, -1, v0
	v_lshrrev_b32_e32 v1, 5, v0
	v_and_b32_e32 v2, 31, v0
	v_lshl_add_u32 v3, s27, 1, v1
	s_lshl_b32 s28, s26, 6
	v_lshl_add_u32 v4, v2, 1, s28
	v_lshlrev_b32_e32 v4, 6, v4
	v_lshl_add_u32 v4, v3, 2, v4
	s_add_u32 s30, s84, 0x1700000
	s_addc_u32 s31, s85, 0
	global_load_dword v5, v4, s[30:31]
	global_load_dword v6, v4, s[30:31] offset:64
	s_and_b32 s34, s26, 127
	s_lshr_b32 s35, s26, 7
	s_lshl_b32 s38, s35, 13
	s_add_u32 s38, s38, 0x8000
	s_add_u32 s38, s84, s38
	s_addc_u32 s39, s85, 0
	v_lshlrev_b32_e32 v10, 6, v2
	v_lshl_add_u32 v10, v3, 3, v10
	v_add_u32_e32 v11, 0x1000, v10
	s_sub_u32 s40, s34, 32
	s_sub_u32 s41, s34, 64
	s_sub_u32 s42, s34, 0x60
	s_mov_b32 s43, 0
.Lfc_poll:
	global_load_dwordx2 v[12:13], v10, s[38:39] sc0 sc1
	global_load_dwordx2 v[14:15], v10, s[38:39] offset:2048 sc0 sc1
	global_load_dwordx2 v[16:17], v11, s[38:39] sc0 sc1
	global_load_dwordx2 v[18:19], v11, s[38:39] offset:2048 sc0 sc1
	s_waitcnt vmcnt(0)
	v_cmp_gt_i32_e32 vcc, s34, v2
	s_nop 1
	v_cndmask_b32_e32 v12, 0, v12, vcc
	v_cndmask_b32_e32 v13, 1, v13, vcc
	v_cmp_gt_i32_e32 vcc, s40, v2
	s_nop 1
	v_cndmask_b32_e32 v14, 0, v14, vcc
	v_cndmask_b32_e32 v15, 1, v15, vcc
	v_cmp_gt_i32_e32 vcc, s41, v2
	s_nop 1
	v_cndmask_b32_e32 v16, 0, v16, vcc
	v_cndmask_b32_e32 v17, 1, v17, vcc
	v_cmp_gt_i32_e32 vcc, s42, v2
	s_nop 1
	v_cndmask_b32_e32 v18, 0, v18, vcc
	v_cndmask_b32_e32 v19, 1, v19, vcc
	v_and_b32_e32 v13, v13, v15
	v_and_b32_e32 v17, v17, v19
	v_and_b32_e32 v13, v13, v17
	v_cmp_ne_u32_e32 vcc, 1, v13
	s_cbranch_vccz .Lfc_ready
	s_sleep 8
	s_add_u32 s43, s43, 1
	s_cmp_lt_u32 s43, 0x4000
	s_cbranch_scc1 .Lfc_poll
.Lfc_ready:
	v_add_f32_e32 v12, v12, v14
	v_add_f32_e32 v16, v16, v18
	v_add_f32_e32 v12, v12, v16
	s_nop 1
	v_add_f32_dpp v12, v12, v12 row_shr:1 row_mask:0xf bank_mask:0xf bound_ctrl:1
	s_nop 1
	v_add_f32_dpp v12, v12, v12 row_shr:2 row_mask:0xf bank_mask:0xf bound_ctrl:1
	s_nop 1
	v_add_f32_dpp v12, v12, v12 row_shr:4 row_mask:0xf bank_mask:0xf bound_ctrl:1
	s_nop 1
	v_add_f32_dpp v12, v12, v12 row_shr:8 row_mask:0xf bank_mask:0xf bound_ctrl:1
	s_nop 1
	v_add_f32_dpp v12, v12, v12 row_bcast:15 row_mask:0xa bank_mask:0xf
	v_add_f32_e32 v7, v5, v6
	s_nop 1
	v_add_f32_dpp v7, v7, v7 row_shr:1 row_mask:0xf bank_mask:0xf bound_ctrl:1
	s_nop 1
	v_add_f32_dpp v7, v7, v7 row_shr:2 row_mask:0xf bank_mask:0xf bound_ctrl:1
	s_nop 1
	v_add_f32_dpp v7, v7, v7 row_shr:4 row_mask:0xf bank_mask:0xf bound_ctrl:1
	s_nop 1
	v_add_f32_dpp v7, v7, v7 row_shr:8 row_mask:0xf bank_mask:0xf bound_ctrl:1
	s_nop 1
	v_add_f32_dpp v7, v7, v7 row_bcast:15 row_mask:0xa bank_mask:0xf
	v_readlane_b32 s0, v12, 31
	v_readlane_b32 s1, v12, 63
	v_cmp_ne_u32_e32 vcc, 0, v1
	v_mov_b32_e32 v20, s0
	v_mov_b32_e32 v21, s1
	v_cndmask_b32_e32 v20, v20, v21, vcc
	v_add_f32_e32 v23, v7, v20
	v_sub_f32_e32 v22, v23, v6
	s_mov_b32 s2, 0xbfb8aa3b
	v_mul_f32_e32 v22, s2, v22
	v_mul_f32_e32 v23, s2, v23
	s_lshl_b32 s3, s35, 18
	s_lshl_b32 s2, s34, 8
	s_add_u32 s2, s2, s3
	s_add_u32 s2, s2, 0x1900000
	s_add_u32 s2, s84, s2
	s_addc_u32 s3, s85, 0
	v_lshlrev_b32_e32 v24, 15, v3
	v_lshl_add_u32 v24, v2, 3, v24
	global_store_dwordx2 v24, v[22:23], s[2:3]
	s_waitcnt vmcnt(0)
	s_waitcnt lgkmcnt(0)
	s_barrier
	s_mov_b64 s[0:1], exec
	v_readlane_b32 s2, v250, 5
	v_readlane_b32 s3, v250, 6
	s_and_b64 s[2:3], s[0:1], s[2:3]
	s_mov_b64 exec, s[2:3]
	s_cbranch_execz .LBB0_1207
	s_add_i32 s2, 0, 0x24000
	v_mov_b32_e32 v0, s2
	s_waitcnt vmcnt(0) expcnt(0) lgkmcnt(0)
	ds_read_b32 v2, v0
	s_add_i32 s2, 0, 0x24004
	v_mov_b32_e32 v0, s2
	ds_read_b32 v0, v0
	s_waitcnt lgkmcnt(1)
	v_cmp_ne_u32_e32 vcc, 0, v2
	s_cbranch_vccnz .LBB0_1171
	s_add_u32 s8, s84, 0x1200
	s_addc_u32 s9, s85, 0
	s_add_u32 s10, s84, 0x1400
	s_addc_u32 s11, s85, 0
	s_add_u32 s12, s84, 0x1500
	s_addc_u32 s13, s85, 0
	s_add_u32 s14, s84, 0x1600
	s_addc_u32 s15, s85, 0
	s_add_u32 s16, s84, 0x1700
	s_addc_u32 s17, s85, 0
	s_add_u32 s24, s84, 0x1800
	s_addc_u32 s25, s85, 0
	s_add_u32 s26, s84, 0x1900
	s_addc_u32 s27, s85, 0
	s_add_u32 s28, s84, 0x1a00
	s_addc_u32 s29, s85, 0
	s_add_u32 s30, s84, 0x1b00
	s_addc_u32 s31, s85, 0
	s_add_u32 s34, s84, 0x1c00
	s_addc_u32 s35, s85, 0
	s_add_u32 s38, s84, 0x1d00
	s_addc_u32 s39, s85, 0
	s_add_u32 s40, s84, 0x1e00
	s_addc_u32 s41, s85, 0
	s_add_u32 s42, s84, 0x1f00
	s_addc_u32 s43, s85, 0
	s_add_u32 s44, s84, 0x2000
	s_addc_u32 s45, s85, 0
	s_add_u32 s48, s84, 0x2100
	s_addc_u32 s49, s85, 0
	s_add_u32 s50, s84, 0x2200
	v_readlane_b32 s2, v250, 2
	s_addc_u32 s51, s85, 0
	s_mul_i32 s2, s87, s2
	s_add_u32 s60, s84, 0x2300
	s_mul_i32 s2, s2, s86
	s_addc_u32 s61, s85, 0
	s_mov_b32 s3, 1
	v_mov_b32_e32 v16, 0
	s_branch .LBB0_1159
